# stack13
# speedup vs baseline: 1.0128x; 1.0092x over previous
.LBB3_10:
	s_cmp_gt_u32 s30, 18
	s_cbranch_scc1 .LBB3_16
	s_ashr_i32 s19, s18, 31
	s_lshl_b64 s[24:25], s[18:19], 15
	v_cndmask_b32_e64 v60, 0, 1, s[20:21]
	v_lshl_add_u64 v[58:59], v[122:123], 0, s[24:25]
	v_lshl_or_b32 v60, v60, 16, v102
	s_mov_b32 s19, 0
	ds_read_b128 v[74:77], v60
	ds_read_b128 v[78:81], v60 offset:8192
	ds_read_b128 v[82:85], v60 offset:16384
	ds_read_b128 v[86:89], v60 offset:24576
	ds_read_b128 v[90:93], v60 offset:32768
	ds_read_b128 v[94:97], v60 offset:40960
	ds_read_b128 v[98:101], v60 offset:49152
	ds_read_b128 v[240:243], v60 offset:57344
	s_waitcnt lgkmcnt(7)
	v_cvt_scalef32_pk_fp8_f16 v70, v74, s63
	v_cvt_scalef32_pk_fp8_f16 v71, v76, s63
	s_waitcnt lgkmcnt(6)
	v_cvt_scalef32_pk_fp8_f16 v72, v78, s63
	v_cvt_scalef32_pk_fp8_f16 v73, v80, s63
	v_cvt_scalef32_pk_fp8_f16 v70, v75, s63 op_sel:[0,0,1]
	v_cvt_scalef32_pk_fp8_f16 v71, v77, s63 op_sel:[0,0,1]
	v_cvt_scalef32_pk_fp8_f16 v72, v79, s63 op_sel:[0,0,1]
	v_cvt_scalef32_pk_fp8_f16 v73, v81, s63 op_sel:[0,0,1]
	global_store_dwordx2 v[58:59], v[70:71], off offset:-4096
	global_store_dwordx2 v[58:59], v[72:73], off
	v_lshl_add_u64 v[58:59], v[58:59], 0, s[22:23]
	s_waitcnt lgkmcnt(5)
	v_cvt_scalef32_pk_fp8_f16 v70, v82, s63
	v_cvt_scalef32_pk_fp8_f16 v71, v84, s63
	s_waitcnt lgkmcnt(4)
	v_cvt_scalef32_pk_fp8_f16 v72, v86, s63
	v_cvt_scalef32_pk_fp8_f16 v73, v88, s63
	v_cvt_scalef32_pk_fp8_f16 v70, v83, s63 op_sel:[0,0,1]
	v_cvt_scalef32_pk_fp8_f16 v71, v85, s63 op_sel:[0,0,1]
	v_cvt_scalef32_pk_fp8_f16 v72, v87, s63 op_sel:[0,0,1]
	v_cvt_scalef32_pk_fp8_f16 v73, v89, s63 op_sel:[0,0,1]
	global_store_dwordx2 v[58:59], v[70:71], off offset:-4096
	global_store_dwordx2 v[58:59], v[72:73], off
	v_lshl_add_u64 v[58:59], v[58:59], 0, s[22:23]
	s_waitcnt lgkmcnt(3)
	v_cvt_scalef32_pk_fp8_f16 v70, v90, s63
	v_cvt_scalef32_pk_fp8_f16 v71, v92, s63
	s_waitcnt lgkmcnt(2)
	v_cvt_scalef32_pk_fp8_f16 v72, v94, s63
	v_cvt_scalef32_pk_fp8_f16 v73, v96, s63
	v_cvt_scalef32_pk_fp8_f16 v70, v91, s63 op_sel:[0,0,1]
	v_cvt_scalef32_pk_fp8_f16 v71, v93, s63 op_sel:[0,0,1]
	v_cvt_scalef32_pk_fp8_f16 v72, v95, s63 op_sel:[0,0,1]
	v_cvt_scalef32_pk_fp8_f16 v73, v97, s63 op_sel:[0,0,1]
	global_store_dwordx2 v[58:59], v[70:71], off offset:-4096
	global_store_dwordx2 v[58:59], v[72:73], off
	v_lshl_add_u64 v[58:59], v[58:59], 0, s[22:23]
	s_waitcnt lgkmcnt(1)
	v_cvt_scalef32_pk_fp8_f16 v70, v98, s63
	v_cvt_scalef32_pk_fp8_f16 v71, v100, s63
	s_waitcnt lgkmcnt(0)
	v_cvt_scalef32_pk_fp8_f16 v72, v240, s63
	v_cvt_scalef32_pk_fp8_f16 v73, v242, s63
	v_cvt_scalef32_pk_fp8_f16 v70, v99, s63 op_sel:[0,0,1]
	v_cvt_scalef32_pk_fp8_f16 v71, v101, s63 op_sel:[0,0,1]
	v_cvt_scalef32_pk_fp8_f16 v72, v241, s63 op_sel:[0,0,1]
	v_cvt_scalef32_pk_fp8_f16 v73, v243, s63 op_sel:[0,0,1]
	global_store_dwordx2 v[58:59], v[70:71], off offset:-4096
	global_store_dwordx2 v[58:59], v[72:73], off
	v_lshl_add_u64 v[58:59], v[58:59], 0, s[22:23]
	s_mov_b64 s[26:27], 0
	s_mov_b64 s[24:25], 0
	s_and_saveexec_b64 s[28:29], s[2:3]
	s_xor_b64 s[28:29], exec, s[28:29]
	s_mov_b64 s[24:25], exec
	v_mul_f32_e32 v58, 0x43800000, v230
	s_or_b64 exec, exec, s[28:29]
	s_branch .LBB3_17
